# E16: E15 + NSA online-softmax rescale v_pk_mul_f32 split into scalar v_mul_f32 pairs (bit-identical) in 5 tile loops
# baseline (speedup 1.0000x reference)
.LBB0_681:
	v_lshlrev_b32_e32 v132, 1, v125
	v_or_b32_e32 v0, 32, v132
	v_or_b32_e32 v68, v0, v163
	s_waitcnt lgkmcnt(0)
	global_load_ushort v68, v68, s[26:27]
	v_or_b32_e32 v0, v0, v164
	s_mov_b32 s37, s90
	s_mov_b32 s2, 0
	s_waitcnt vmcnt(0)
	v_lshlrev_b32_e32 v68, 16, v68
	v_mul_f32_e32 v68, 0xbfb8aa3b, v68
	v_exp_f32_e32 v68, v68
	s_nop 0
	v_add_f32_e32 v68, 1.0, v68
	v_div_scale_f32 v69, s[0:1], v68, v68, 1.0
	v_rcp_f32_e32 v70, v69
	s_nop 0
	v_fma_f32 v71, -v69, v70, 1.0
	v_fmac_f32_e32 v70, v71, v70
	v_div_scale_f32 v71, vcc, 1.0, v68, 1.0
	v_mul_f32_e32 v72, v71, v70
	v_fma_f32 v73, -v69, v72, v71
	v_fmac_f32_e32 v72, v73, v70
	v_fma_f32 v69, -v69, v72, v71
	v_div_fmas_f32 v69, v69, v70, v72
	v_div_fixup_f32 v68, v69, v68, 1.0
	v_mul_f32_e32 v66, v66, v68
	v_mul_f32_e32 v67, v67, v68
	v_mul_f32_e32 v64, v64, v68
	v_mul_f32_e32 v65, v65, v68
	v_mul_f32_e32 v62, v62, v68
	v_mul_f32_e32 v63, v63, v68
	v_cvt_pk_bf16_f32 v64, v64, v65
	v_cvt_pk_bf16_f32 v65, v66, v67
	v_or_b32_e32 v66, 0x800, v2
	v_mul_f32_e32 v60, v60, v68
	v_mul_f32_e32 v61, v61, v68
	v_mul_f32_e32 v58, v58, v68
	v_mul_f32_e32 v59, v59, v68
	v_mul_f32_e32 v56, v56, v68
	v_mul_f32_e32 v57, v57, v68
	v_mul_f32_e32 v54, v54, v68
	v_mul_f32_e32 v55, v55, v68
	v_mul_f32_e32 v52, v52, v68
	v_mul_f32_e32 v53, v53, v68
	v_mul_f32_e32 v50, v50, v68
	v_mul_f32_e32 v51, v51, v68
	v_mul_f32_e32 v48, v48, v68
	v_mul_f32_e32 v49, v49, v68
	v_mul_f32_e32 v46, v46, v68
	v_mul_f32_e32 v47, v47, v68
	v_mul_f32_e32 v44, v44, v68
	v_mul_f32_e32 v45, v45, v68
	v_mul_f32_e32 v42, v42, v68
	v_mul_f32_e32 v43, v43, v68
	v_mul_f32_e32 v40, v40, v68
	v_mul_f32_e32 v41, v41, v68
	v_mul_f32_e32 v38, v38, v68
	v_mul_f32_e32 v39, v39, v68
	v_mul_f32_e32 v36, v36, v68
	v_mul_f32_e32 v37, v37, v68
	v_or_b32_e32 v2, v66, v193
	v_cvt_pk_bf16_f32 v60, v60, v61
	v_cvt_pk_bf16_f32 v61, v62, v63
	v_cvt_pk_bf16_f32 v56, v56, v57
	v_cvt_pk_bf16_f32 v57, v58, v59
	v_cvt_pk_bf16_f32 v52, v52, v53
	v_cvt_pk_bf16_f32 v53, v54, v55
	v_cvt_pk_bf16_f32 v48, v48, v49
	v_cvt_pk_bf16_f32 v49, v50, v51
	v_cvt_pk_bf16_f32 v44, v44, v45
	v_cvt_pk_bf16_f32 v45, v46, v47
	v_cvt_pk_bf16_f32 v40, v40, v41
	v_cvt_pk_bf16_f32 v41, v42, v43
	v_cvt_pk_bf16_f32 v36, v36, v37
	v_cvt_pk_bf16_f32 v37, v38, v39
	global_store_dwordx2 v2, v[64:65], s[24:25]
	global_store_dwordx2 v2, v[60:61], s[24:25] offset:32
	global_store_dwordx2 v2, v[56:57], s[24:25] offset:64
	global_store_dwordx2 v2, v[52:53], s[24:25] offset:96
	global_store_dwordx2 v2, v[48:49], s[24:25] offset:128
	global_store_dwordx2 v2, v[44:45], s[24:25] offset:160
	global_store_dwordx2 v2, v[40:41], s[24:25] offset:192
	global_store_dwordx2 v2, v[36:37], s[24:25] offset:224
	global_load_ushort v0, v0, s[26:27]
	v_lshl_add_u64 v[130:131], s[24:25], 0, v[2:3]
	s_waitcnt vmcnt(0)
	v_lshlrev_b32_e32 v0, 16, v0
	v_mul_f32_e32 v0, 0xbfb8aa3b, v0
	v_exp_f32_e32 v0, v0
	s_nop 0
	v_add_f32_e32 v0, 1.0, v0
	v_div_scale_f32 v2, s[0:1], v0, v0, 1.0
	v_rcp_f32_e32 v36, v2
	s_mov_b32 s0, -1
	s_mov_b32 s1, 0
	v_fma_f32 v37, -v2, v36, 1.0
	v_fmac_f32_e32 v36, v37, v36
	v_div_scale_f32 v37, vcc, 1.0, v0, 1.0
	v_mul_f32_e32 v38, v37, v36
	v_fma_f32 v39, -v2, v38, v37
	v_fmac_f32_e32 v38, v39, v36
	v_fma_f32 v2, -v2, v38, v37
	v_div_fmas_f32 v2, v2, v36, v38
	v_div_fixup_f32 v36, v2, v0, 1.0
	v_mul_f32_e32 v34, v34, v36
	v_mul_f32_e32 v35, v35, v36
	v_mul_f32_e32 v32, v32, v36
	v_mul_f32_e32 v33, v33, v36
	v_or_b32_e32 v2, v66, v194
	v_mul_f32_e32 v30, v30, v36
	v_mul_f32_e32 v31, v31, v36
	v_mul_f32_e32 v28, v28, v36
	v_mul_f32_e32 v29, v29, v36
	v_mul_f32_e32 v26, v26, v36
	v_mul_f32_e32 v27, v27, v36
	v_mul_f32_e32 v24, v24, v36
	v_mul_f32_e32 v25, v25, v36
	v_mul_f32_e32 v22, v22, v36
	v_mul_f32_e32 v23, v23, v36
	v_mul_f32_e32 v20, v20, v36
	v_mul_f32_e32 v21, v21, v36
	v_mul_f32_e32 v18, v18, v36
	v_mul_f32_e32 v19, v19, v36
	v_mul_f32_e32 v16, v16, v36
	v_mul_f32_e32 v17, v17, v36
	v_mul_f32_e32 v14, v14, v36
	v_mul_f32_e32 v15, v15, v36
	v_mul_f32_e32 v12, v12, v36
	v_mul_f32_e32 v13, v13, v36
	v_mul_f32_e32 v10, v10, v36
	v_mul_f32_e32 v11, v11, v36
	v_mul_f32_e32 v8, v8, v36
	v_mul_f32_e32 v9, v9, v36
	v_mul_f32_e32 v6, v6, v36
	v_mul_f32_e32 v7, v7, v36
	v_mul_f32_e32 v4, v4, v36
	v_mul_f32_e32 v5, v5, v36
	v_cvt_pk_bf16_f32 v32, v32, v33
	v_cvt_pk_bf16_f32 v33, v34, v35
	v_lshl_add_u64 v[128:129], s[24:25], 0, v[2:3]
	v_cvt_pk_bf16_f32 v28, v28, v29
	v_cvt_pk_bf16_f32 v29, v30, v31
	v_cvt_pk_bf16_f32 v24, v24, v25
	v_cvt_pk_bf16_f32 v25, v26, v27
	v_cvt_pk_bf16_f32 v20, v20, v21
	v_cvt_pk_bf16_f32 v21, v22, v23
	v_cvt_pk_bf16_f32 v16, v16, v17
	v_cvt_pk_bf16_f32 v17, v18, v19
	v_cvt_pk_bf16_f32 v12, v12, v13
	v_cvt_pk_bf16_f32 v13, v14, v15
	v_cvt_pk_bf16_f32 v8, v8, v9
	v_cvt_pk_bf16_f32 v9, v10, v11
	v_cvt_pk_bf16_f32 v4, v4, v5
	v_cvt_pk_bf16_f32 v5, v6, v7
	global_store_dwordx2 v2, v[32:33], s[24:25]
	global_store_dwordx2 v2, v[28:29], s[24:25] offset:32
	global_store_dwordx2 v2, v[24:25], s[24:25] offset:64
	global_store_dwordx2 v2, v[20:21], s[24:25] offset:96
	global_store_dwordx2 v2, v[16:17], s[24:25] offset:128
	global_store_dwordx2 v2, v[12:13], s[24:25] offset:160
	global_store_dwordx2 v2, v[8:9], s[24:25] offset:192
	global_store_dwordx2 v2, v[4:5], s[24:25] offset:224

.Lr687_skip:
	s_waitcnt lgkmcnt(0)
	v_mfma_f32_16x16x32_bf16 v[90:93], v[70:73], v[78:81], 0
	v_mfma_f32_16x16x32_bf16 v[70:73], v[70:73], v[82:85], 0
	v_add_u32_e32 v0, s0, v143
	ds_read_b128 v[198:201], v0
	ds_read_b128 v[202:205], v197 offset:1024
	ds_read_b128 v[206:209], v197 offset:5120
	v_mfma_f32_16x16x32_bf16 v[98:101], v[74:77], v[78:81], 0
	v_mfma_f32_16x16x32_bf16 v[74:77], v[74:77], v[82:85], 0
	v_mfma_f32_16x16x32_bf16 v[210:213], v[86:89], v[78:81], 0
	ds_read_b128 v[214:217], v0 offset:4096
	v_mfma_f32_16x16x32_bf16 v[86:89], v[86:89], v[82:85], 0
	v_mfma_f32_16x16x32_bf16 v[78:81], v[94:97], v[78:81], 0
	v_mfma_f32_16x16x32_bf16 v[82:85], v[94:97], v[82:85], 0
	ds_read_b128 v[94:97], v0 offset:8192
	s_waitcnt lgkmcnt(3)
	v_mfma_f32_16x16x32_bf16 v[90:93], v[198:201], v[202:205], v[90:93]
	s_waitcnt lgkmcnt(2)
	v_mfma_f32_16x16x32_bf16 v[70:73], v[198:201], v[206:209], v[70:73]
	ds_read_b128 v[198:201], v0 offset:12288
	v_add_u32_e32 v0, s0, v144
	s_waitcnt lgkmcnt(2)
	v_mfma_f32_16x16x32_bf16 v[98:101], v[214:217], v[202:205], v[98:101]
	v_mfma_f32_16x16x32_bf16 v[74:77], v[214:217], v[206:209], v[74:77]
	ds_read_b128 v[214:217], v0
	ds_read_b128 v[218:221], v197 offset:2048
	ds_read_b128 v[222:225], v197 offset:6144
	s_waitcnt lgkmcnt(4)
	v_mfma_f32_16x16x32_bf16 v[210:213], v[94:97], v[202:205], v[210:213]
	v_mfma_f32_16x16x32_bf16 v[86:89], v[94:97], v[206:209], v[86:89]
	ds_read_b128 v[94:97], v0 offset:4096
	s_waitcnt lgkmcnt(4)
	v_mfma_f32_16x16x32_bf16 v[78:81], v[198:201], v[202:205], v[78:81]
	ds_read_b128 v[202:205], v0 offset:8192
	v_mfma_f32_16x16x32_bf16 v[82:85], v[198:201], v[206:209], v[82:85]
	s_waitcnt lgkmcnt(3)
	v_mfma_f32_16x16x32_bf16 v[90:93], v[214:217], v[218:221], v[90:93]
	ds_read_b128 v[198:201], v0 offset:12288
	s_waitcnt lgkmcnt(3)
	v_mfma_f32_16x16x32_bf16 v[70:73], v[214:217], v[222:225], v[70:73]
	v_add_u32_e32 v0, s0, v145
	s_waitcnt lgkmcnt(2)
	v_mfma_f32_16x16x32_bf16 v[206:209], v[94:97], v[218:221], v[98:101]
	v_mfma_f32_16x16x32_bf16 v[74:77], v[94:97], v[222:225], v[74:77]
	ds_read_b128 v[94:97], v0
	ds_read_b128 v[214:217], v197 offset:3072
	ds_read_b128 v[228:231], v197 offset:7168
	s_waitcnt lgkmcnt(4)
	v_mfma_f32_16x16x32_bf16 v[210:213], v[202:205], v[218:221], v[210:213]
	v_mfma_f32_16x16x32_bf16 v[86:89], v[202:205], v[222:225], v[86:89]
	ds_read_b128 v[202:205], v0 offset:4096
	ds_read_b128 v[232:235], v0 offset:8192
	s_waitcnt lgkmcnt(5)
	v_mfma_f32_16x16x32_bf16 v[218:221], v[198:201], v[218:221], v[78:81]
	v_mfma_f32_16x16x32_bf16 v[198:201], v[198:201], v[222:225], v[82:85]
	s_waitcnt lgkmcnt(3)
	v_mfma_f32_16x16x32_bf16 v[82:85], v[94:97], v[214:217], v[90:93]
	ds_read_b128 v[222:225], v0 offset:12288
	s_waitcnt lgkmcnt(3)
	v_mfma_f32_16x16x32_bf16 v[98:101], v[94:97], v[228:231], v[70:73]
	s_waitcnt lgkmcnt(2)
	v_mfma_f32_16x16x32_bf16 v[78:81], v[202:205], v[214:217], v[206:209]
	v_mfma_f32_16x16x32_bf16 v[94:97], v[202:205], v[228:231], v[74:77]
	s_waitcnt lgkmcnt(1)
	v_mfma_f32_16x16x32_bf16 v[74:77], v[232:235], v[214:217], v[210:213]
	v_mfma_f32_16x16x32_bf16 v[90:93], v[232:235], v[228:231], v[86:89]
	s_nop 0
	v_max_f32_e32 v2, v82, v83
	s_waitcnt lgkmcnt(0)
	v_mfma_f32_16x16x32_bf16 v[70:73], v[222:225], v[214:217], v[218:221]
	s_ashr_i32 s22, s1, 5
	v_max_f32_e32 v125, v84, v85
	v_mfma_f32_16x16x32_bf16 v[86:89], v[222:225], v[228:231], v[198:201]
	v_lshl_add_u32 v134, s22, 2, v148
	ds_read_b32 v5, v196 offset:508
	ds_read_b32 v0, v134
	v_max_f32_e32 v137, v80, v81
	v_max3_f32 v137, v78, v79, v137
	v_max3_f32 v2, v2, v125, v137
	v_max_f32_e32 v125, v76, v77
	v_max_f32_e32 v137, v72, v73
	s_lshl_b32 s0, 1, s1
	v_max3_f32 v125, v74, v75, v125
	v_max3_f32 v137, v70, v71, v137
	s_waitcnt lgkmcnt(0)
	v_and_b32_e32 v0, s0, v0
	v_max3_f32 v2, v2, v125, v137
	v_cmp_ne_u32_e32 vcc, 0, v0
	v_mov_b32_e32 v0, v2
	s_nop 1
	v_permlane16_swap_b32_e32 v2, v0
	v_max_f32_e32 v0, v2, v0
	v_mov_b32_e32 v2, v0
	s_nop 1
	v_permlane32_swap_b32_e32 v0, v2
	v_cndmask_b32_e32 v137, v159, v5, vcc
	v_max_f32_e32 v0, v0, v2
	v_fmamk_f32 v0, v0, 0x3fb8aa3b, v137
	v_max_f32_e32 v125, v133, v0
	v_sub_f32_e32 v0, v133, v125
	v_exp_f32_e32 v2, v0
	s_nop 0
	v_cmp_neq_f32_e32 vcc, 1.0, v2
	s_cbranch_vccz .LBB0_695
	v_mul_f32_e32 v68, v68, v2
	v_mul_f32_e32 v69, v69, v2
	v_mul_f32_e32 v66, v66, v2
	v_mul_f32_e32 v67, v67, v2
	v_mul_f32_e32 v64, v64, v2
	v_mul_f32_e32 v65, v65, v2
	v_mul_f32_e32 v62, v62, v2
	v_mul_f32_e32 v63, v63, v2
	v_mul_f32_e32 v60, v60, v2
	v_mul_f32_e32 v61, v61, v2
	v_mul_f32_e32 v58, v58, v2
	v_mul_f32_e32 v59, v59, v2
	v_mul_f32_e32 v56, v56, v2
	v_mul_f32_e32 v57, v57, v2
	v_mul_f32_e32 v54, v54, v2
	v_mul_f32_e32 v55, v55, v2
	v_mul_f32_e32 v52, v52, v2
	v_mul_f32_e32 v53, v53, v2
	v_mul_f32_e32 v50, v50, v2
	v_mul_f32_e32 v51, v51, v2
	v_mul_f32_e32 v48, v48, v2
	v_mul_f32_e32 v49, v49, v2
	v_mul_f32_e32 v46, v46, v2
	v_mul_f32_e32 v47, v47, v2
	v_mul_f32_e32 v44, v44, v2
	v_mul_f32_e32 v45, v45, v2
	v_mul_f32_e32 v42, v42, v2
	v_mul_f32_e32 v43, v43, v2
	v_mul_f32_e32 v40, v40, v2
	v_mul_f32_e32 v41, v41, v2
	v_mul_f32_e32 v38, v38, v2
	v_mul_f32_e32 v39, v39, v2
.LBB0_695:
	ds_read_b32 v0, v134 offset:32
	v_max_f32_e32 v133, v98, v99
	v_max_f32_e32 v134, v100, v101
	v_max_f32_e32 v198, v96, v97
	v_max3_f32 v198, v94, v95, v198
	v_max3_f32 v133, v133, v134, v198
	v_max_f32_e32 v134, v92, v93
	v_max_f32_e32 v198, v88, v89
	v_max3_f32 v134, v90, v91, v134
	v_max3_f32 v198, v86, v87, v198
	s_waitcnt lgkmcnt(0)
	v_and_b32_e32 v0, s0, v0
	v_max3_f32 v133, v133, v134, v198
	v_cmp_ne_u32_e32 vcc, 0, v0
	v_mov_b32_e32 v0, v133
	s_nop 1
	v_permlane16_swap_b32_e32 v133, v0
	v_max_f32_e32 v0, v133, v0
	v_mov_b32_e32 v133, v0
	s_nop 1
	v_permlane32_swap_b32_e32 v0, v133
	v_cndmask_b32_e32 v5, v159, v5, vcc
	v_max_f32_e32 v0, v0, v133
	v_fmamk_f32 v0, v0, 0x3fb8aa3b, v5
	v_max_f32_e32 v134, v4, v0
	v_sub_f32_e32 v0, v4, v134
	v_exp_f32_e32 v4, v0
	s_nop 0
	v_cmp_neq_f32_e32 vcc, 1.0, v4
	s_cbranch_vccz .LBB0_697
	v_mul_f32_e32 v36, v36, v4
	v_mul_f32_e32 v37, v37, v4
	v_mul_f32_e32 v34, v34, v4
	v_mul_f32_e32 v35, v35, v4
	v_mul_f32_e32 v32, v32, v4
	v_mul_f32_e32 v33, v33, v4
	v_mul_f32_e32 v30, v30, v4
	v_mul_f32_e32 v31, v31, v4
	v_mul_f32_e32 v28, v28, v4
	v_mul_f32_e32 v29, v29, v4
	v_mul_f32_e32 v26, v26, v4
	v_mul_f32_e32 v27, v27, v4
	v_mul_f32_e32 v24, v24, v4
	v_mul_f32_e32 v25, v25, v4
	v_mul_f32_e32 v22, v22, v4
	v_mul_f32_e32 v23, v23, v4
	v_mul_f32_e32 v20, v20, v4
	v_mul_f32_e32 v21, v21, v4
	v_mul_f32_e32 v18, v18, v4
	v_mul_f32_e32 v19, v19, v4
	v_mul_f32_e32 v16, v16, v4
	v_mul_f32_e32 v17, v17, v4
	v_mul_f32_e32 v14, v14, v4
	v_mul_f32_e32 v15, v15, v4
	v_mul_f32_e32 v12, v12, v4
	v_mul_f32_e32 v13, v13, v4
	v_mul_f32_e32 v10, v10, v4
	v_mul_f32_e32 v11, v11, v4
	v_mul_f32_e32 v8, v8, v4
	v_mul_f32_e32 v9, v9, v4
	v_mul_f32_e32 v6, v6, v4
	v_mul_f32_e32 v7, v7, v4

.LBB0_776:
	s_or_b64 exec, exec, s[0:1]
	v_max_f32_e32 v0, v136, v135
	v_max3_f32 v0, v0, v99, v98
	v_max3_f32 v0, v0, v101, v100
	v_max3_f32 v0, v0, v95, v94
	v_max3_f32 v0, v0, v97, v96
	v_max3_f32 v0, v0, v91, v90
	v_max3_f32 v0, v0, v93, v92
	v_max3_f32 v0, v0, v87, v86
	v_mov_b32_e32 v2, v0
	s_nop 1
	v_permlane16_swap_b32_e32 v0, v2
	v_max_f32_e32 v0, v0, v2
	v_mov_b32_e32 v2, v0
	s_nop 1
	v_permlane32_swap_b32_e32 v0, v2
	v_max3_f32 v71, v125, v0, v2
	v_sub_f32_e32 v0, v125, v71
	v_exp_f32_e32 v2, v0
	s_nop 0
	v_cmp_neq_f32_e32 vcc, 1.0, v2
	s_cbranch_vccz .LBB0_778
	v_mul_f32_e32 v68, v68, v2
	v_mul_f32_e32 v69, v69, v2
	v_mul_f32_e32 v66, v66, v2
	v_mul_f32_e32 v67, v67, v2
	v_mul_f32_e32 v64, v64, v2
	v_mul_f32_e32 v65, v65, v2
	v_mul_f32_e32 v62, v62, v2
	v_mul_f32_e32 v63, v63, v2
	v_mul_f32_e32 v60, v60, v2
	v_mul_f32_e32 v61, v61, v2
	v_mul_f32_e32 v58, v58, v2
	v_mul_f32_e32 v59, v59, v2
	v_mul_f32_e32 v56, v56, v2
	v_mul_f32_e32 v57, v57, v2
	v_mul_f32_e32 v54, v54, v2
	v_mul_f32_e32 v55, v55, v2
	v_mul_f32_e32 v52, v52, v2
	v_mul_f32_e32 v53, v53, v2
	v_mul_f32_e32 v50, v50, v2
	v_mul_f32_e32 v51, v51, v2
	v_mul_f32_e32 v48, v48, v2
	v_mul_f32_e32 v49, v49, v2
	v_mul_f32_e32 v46, v46, v2
	v_mul_f32_e32 v47, v47, v2
	v_mul_f32_e32 v44, v44, v2
	v_mul_f32_e32 v45, v45, v2
	v_mul_f32_e32 v42, v42, v2
	v_mul_f32_e32 v43, v43, v2
	v_mul_f32_e32 v40, v40, v2
	v_mul_f32_e32 v41, v41, v2
	v_mul_f32_e32 v38, v38, v2
	v_mul_f32_e32 v39, v39, v2
.LBB0_778:
	v_max_f32_e32 v0, v89, v88
	v_max3_f32 v0, v0, v83, v82
	v_max3_f32 v0, v0, v85, v84
	v_max3_f32 v0, v0, v79, v78
	v_max3_f32 v0, v0, v81, v80
	v_max3_f32 v0, v0, v75, v74
	v_max3_f32 v0, v0, v77, v76
	v_max3_f32 v0, v0, v137, v70
	v_mov_b32_e32 v4, v0
	s_nop 1
	v_permlane16_swap_b32_e32 v0, v4
	v_max_f32_e32 v0, v0, v4
	v_mov_b32_e32 v4, v0
	s_nop 1
	v_permlane32_swap_b32_e32 v0, v4
	v_max3_f32 v72, v134, v0, v4
	v_sub_f32_e32 v0, v134, v72
	v_exp_f32_e32 v4, v0
	s_nop 0
	v_cmp_neq_f32_e32 vcc, 1.0, v4
	s_cbranch_vccz .LBB0_780
	v_mul_f32_e32 v36, v36, v4
	v_mul_f32_e32 v37, v37, v4
	v_mul_f32_e32 v34, v34, v4
	v_mul_f32_e32 v35, v35, v4
	v_mul_f32_e32 v32, v32, v4
	v_mul_f32_e32 v33, v33, v4
	v_mul_f32_e32 v30, v30, v4
	v_mul_f32_e32 v31, v31, v4
	v_mul_f32_e32 v28, v28, v4
	v_mul_f32_e32 v29, v29, v4
	v_mul_f32_e32 v26, v26, v4
	v_mul_f32_e32 v27, v27, v4
	v_mul_f32_e32 v24, v24, v4
	v_mul_f32_e32 v25, v25, v4
	v_mul_f32_e32 v22, v22, v4
	v_mul_f32_e32 v23, v23, v4
	v_mul_f32_e32 v20, v20, v4
	v_mul_f32_e32 v21, v21, v4
	v_mul_f32_e32 v18, v18, v4
	v_mul_f32_e32 v19, v19, v4
	v_mul_f32_e32 v16, v16, v4
	v_mul_f32_e32 v17, v17, v4
	v_mul_f32_e32 v14, v14, v4
	v_mul_f32_e32 v15, v15, v4
	v_mul_f32_e32 v12, v12, v4
	v_mul_f32_e32 v13, v13, v4
	v_mul_f32_e32 v10, v10, v4
	v_mul_f32_e32 v11, v11, v4
	v_mul_f32_e32 v8, v8, v4
	v_mul_f32_e32 v9, v9, v4
	v_mul_f32_e32 v6, v6, v4
	v_mul_f32_e32 v7, v7, v4

.LBB0_801:
	s_lshl_b32 s0, s81, 14
	s_add_i32 s0, s0, 0
	v_add_u32_e32 v0, s0, v140
	ds_read_b128 v[70:73], v0
	ds_read_b128 v[74:77], v0 offset:4096
	ds_read_b128 v[78:81], v197
	ds_read_b128 v[82:85], v197 offset:4096
	ds_read_b128 v[86:89], v0 offset:8192
	ds_read_b128 v[94:97], v0 offset:12288
	s_waitcnt lgkmcnt(0)
	v_mfma_f32_16x16x32_bf16 v[90:93], v[70:73], v[78:81], 0
	v_mfma_f32_16x16x32_bf16 v[70:73], v[70:73], v[82:85], 0
	v_add_u32_e32 v0, s0, v143
	ds_read_b128 v[198:201], v0
	ds_read_b128 v[202:205], v197 offset:1024
	ds_read_b128 v[206:209], v197 offset:5120
	v_mfma_f32_16x16x32_bf16 v[98:101], v[74:77], v[78:81], 0
	v_mfma_f32_16x16x32_bf16 v[74:77], v[74:77], v[82:85], 0
	v_mfma_f32_16x16x32_bf16 v[210:213], v[86:89], v[78:81], 0
	ds_read_b128 v[214:217], v0 offset:4096
	v_mfma_f32_16x16x32_bf16 v[86:89], v[86:89], v[82:85], 0
	v_mfma_f32_16x16x32_bf16 v[78:81], v[94:97], v[78:81], 0
	v_mfma_f32_16x16x32_bf16 v[82:85], v[94:97], v[82:85], 0
	ds_read_b128 v[94:97], v0 offset:8192
	s_waitcnt lgkmcnt(3)
	v_mfma_f32_16x16x32_bf16 v[90:93], v[198:201], v[202:205], v[90:93]
	s_waitcnt lgkmcnt(2)
	v_mfma_f32_16x16x32_bf16 v[70:73], v[198:201], v[206:209], v[70:73]
	ds_read_b128 v[198:201], v0 offset:12288
	v_add_u32_e32 v0, s0, v144
	s_waitcnt lgkmcnt(2)
	v_mfma_f32_16x16x32_bf16 v[98:101], v[214:217], v[202:205], v[98:101]
	v_mfma_f32_16x16x32_bf16 v[74:77], v[214:217], v[206:209], v[74:77]
	ds_read_b128 v[214:217], v0
	ds_read_b128 v[218:221], v197 offset:2048
	ds_read_b128 v[222:225], v197 offset:6144
	s_waitcnt lgkmcnt(4)
	v_mfma_f32_16x16x32_bf16 v[210:213], v[94:97], v[202:205], v[210:213]
	v_mfma_f32_16x16x32_bf16 v[86:89], v[94:97], v[206:209], v[86:89]
	ds_read_b128 v[94:97], v0 offset:4096
	s_waitcnt lgkmcnt(4)
	v_mfma_f32_16x16x32_bf16 v[78:81], v[198:201], v[202:205], v[78:81]
	ds_read_b128 v[202:205], v0 offset:8192
	v_mfma_f32_16x16x32_bf16 v[82:85], v[198:201], v[206:209], v[82:85]
	s_waitcnt lgkmcnt(3)
	v_mfma_f32_16x16x32_bf16 v[90:93], v[214:217], v[218:221], v[90:93]
	ds_read_b128 v[198:201], v0 offset:12288
	s_waitcnt lgkmcnt(3)
	v_mfma_f32_16x16x32_bf16 v[70:73], v[214:217], v[222:225], v[70:73]
	v_add_u32_e32 v0, s0, v145
	s_waitcnt lgkmcnt(2)
	v_mfma_f32_16x16x32_bf16 v[206:209], v[94:97], v[218:221], v[98:101]
	v_mfma_f32_16x16x32_bf16 v[74:77], v[94:97], v[222:225], v[74:77]
	ds_read_b128 v[94:97], v0
	ds_read_b128 v[214:217], v197 offset:3072
	ds_read_b128 v[228:231], v197 offset:7168
	s_waitcnt lgkmcnt(4)
	v_mfma_f32_16x16x32_bf16 v[210:213], v[202:205], v[218:221], v[210:213]
	v_mfma_f32_16x16x32_bf16 v[86:89], v[202:205], v[222:225], v[86:89]
	ds_read_b128 v[202:205], v0 offset:4096
	ds_read_b128 v[232:235], v0 offset:8192
	s_waitcnt lgkmcnt(5)
	v_mfma_f32_16x16x32_bf16 v[218:221], v[198:201], v[218:221], v[78:81]
	v_mfma_f32_16x16x32_bf16 v[198:201], v[198:201], v[222:225], v[82:85]
	s_waitcnt lgkmcnt(3)
	v_mfma_f32_16x16x32_bf16 v[82:85], v[94:97], v[214:217], v[90:93]
	ds_read_b128 v[222:225], v0 offset:12288
	s_waitcnt lgkmcnt(3)
	v_mfma_f32_16x16x32_bf16 v[98:101], v[94:97], v[228:231], v[70:73]
	s_waitcnt lgkmcnt(2)
	v_mfma_f32_16x16x32_bf16 v[78:81], v[202:205], v[214:217], v[206:209]
	v_mfma_f32_16x16x32_bf16 v[94:97], v[202:205], v[228:231], v[74:77]
	s_waitcnt lgkmcnt(1)
	v_mfma_f32_16x16x32_bf16 v[74:77], v[232:235], v[214:217], v[210:213]
	v_mfma_f32_16x16x32_bf16 v[90:93], v[232:235], v[228:231], v[86:89]
	s_nop 0
	v_max_f32_e32 v0, v82, v83
	s_waitcnt lgkmcnt(0)
	v_mfma_f32_16x16x32_bf16 v[70:73], v[222:225], v[214:217], v[218:221]
	v_max_f32_e32 v2, v84, v85
	s_nop 0
	v_max_f32_e32 v5, v80, v81
	v_max3_f32 v5, v78, v79, v5
	v_max3_f32 v0, v0, v2, v5
	v_max_f32_e32 v2, v76, v77
	s_nop 1
	v_max_f32_e32 v5, v72, v73
	v_max3_f32 v2, v74, v75, v2
	v_max3_f32 v5, v70, v71, v5
	v_max3_f32 v0, v0, v2, v5
	v_mov_b32_e32 v2, v0
	s_nop 1
	v_permlane16_swap_b32_e32 v0, v2
	ds_read_b32 v125, v196 offset:508
	v_max_f32_e32 v0, v0, v2
	v_mov_b32_e32 v2, v0
	s_nop 1
	v_permlane32_swap_b32_e32 v0, v2
	v_max_f32_e32 v0, v0, v2
	s_waitcnt lgkmcnt(0)
	v_fmamk_f32 v0, v0, 0x3fb8aa3b, v125
	v_max_f32_e32 v133, v137, v0
	v_sub_f32_e32 v0, v137, v133
	v_exp_f32_e32 v2, v0
	v_mfma_f32_16x16x32_bf16 v[86:89], v[222:225], v[228:231], v[198:201]
	v_cmp_neq_f32_e32 vcc, 1.0, v2
	s_cbranch_vccz .LBB0_803
	v_mul_f32_e32 v68, v68, v2
	v_mul_f32_e32 v69, v69, v2
	v_mul_f32_e32 v66, v66, v2
	v_mul_f32_e32 v67, v67, v2
	v_mul_f32_e32 v64, v64, v2
	v_mul_f32_e32 v65, v65, v2
	v_mul_f32_e32 v62, v62, v2
	v_mul_f32_e32 v63, v63, v2
	v_mul_f32_e32 v60, v60, v2
	v_mul_f32_e32 v61, v61, v2
	v_mul_f32_e32 v58, v58, v2
	v_mul_f32_e32 v59, v59, v2
	v_mul_f32_e32 v56, v56, v2
	v_mul_f32_e32 v57, v57, v2
	v_mul_f32_e32 v54, v54, v2
	v_mul_f32_e32 v55, v55, v2
	v_mul_f32_e32 v52, v52, v2
	v_mul_f32_e32 v53, v53, v2
	v_mul_f32_e32 v50, v50, v2
	v_mul_f32_e32 v51, v51, v2
	v_mul_f32_e32 v48, v48, v2
	v_mul_f32_e32 v49, v49, v2
	v_mul_f32_e32 v46, v46, v2
	v_mul_f32_e32 v47, v47, v2
	v_mul_f32_e32 v44, v44, v2
	v_mul_f32_e32 v45, v45, v2
	v_mul_f32_e32 v42, v42, v2
	v_mul_f32_e32 v43, v43, v2
	v_mul_f32_e32 v40, v40, v2
	v_mul_f32_e32 v41, v41, v2
	v_mul_f32_e32 v38, v38, v2
	v_mul_f32_e32 v39, v39, v2
.LBB0_803:
	v_max_f32_e32 v0, v98, v99
	v_max_f32_e32 v5, v100, v101
	v_max_f32_e32 v134, v96, v97
	v_max3_f32 v134, v94, v95, v134
	v_max3_f32 v0, v0, v5, v134
	v_max_f32_e32 v5, v92, v93
	v_max_f32_e32 v134, v88, v89
	v_max3_f32 v5, v90, v91, v5
	v_max3_f32 v134, v86, v87, v134
	v_max3_f32 v0, v0, v5, v134
	v_mov_b32_e32 v5, v0
	s_nop 1
	v_permlane16_swap_b32_e32 v0, v5
	v_max_f32_e32 v0, v0, v5
	v_mov_b32_e32 v5, v0
	s_nop 1
	v_permlane32_swap_b32_e32 v0, v5
	v_max_f32_e32 v0, v0, v5
	v_fmamk_f32 v0, v0, 0x3fb8aa3b, v125
	v_max_f32_e32 v5, v4, v4
	v_max_f32_e32 v134, v5, v0
	v_sub_f32_e32 v0, v4, v134
	v_exp_f32_e32 v4, v0
	s_nop 0
	v_cmp_neq_f32_e32 vcc, 1.0, v4
	s_cbranch_vccz .LBB0_805
	v_mul_f32_e32 v36, v36, v4
	v_mul_f32_e32 v37, v37, v4
	v_mul_f32_e32 v34, v34, v4
	v_mul_f32_e32 v35, v35, v4
	v_mul_f32_e32 v32, v32, v4
	v_mul_f32_e32 v33, v33, v4
	v_mul_f32_e32 v30, v30, v4
	v_mul_f32_e32 v31, v31, v4
	v_mul_f32_e32 v28, v28, v4
	v_mul_f32_e32 v29, v29, v4
	v_mul_f32_e32 v26, v26, v4
	v_mul_f32_e32 v27, v27, v4
	v_mul_f32_e32 v24, v24, v4
	v_mul_f32_e32 v25, v25, v4
	v_mul_f32_e32 v22, v22, v4
	v_mul_f32_e32 v23, v23, v4
	v_mul_f32_e32 v20, v20, v4
	v_mul_f32_e32 v21, v21, v4
	v_mul_f32_e32 v18, v18, v4
	v_mul_f32_e32 v19, v19, v4
	v_mul_f32_e32 v16, v16, v4
	v_mul_f32_e32 v17, v17, v4
	v_mul_f32_e32 v14, v14, v4
	v_mul_f32_e32 v15, v15, v4
	v_mul_f32_e32 v12, v12, v4
	v_mul_f32_e32 v13, v13, v4
	v_mul_f32_e32 v10, v10, v4
	v_mul_f32_e32 v11, v11, v4
	v_mul_f32_e32 v8, v8, v4
	v_mul_f32_e32 v9, v9, v4
	v_mul_f32_e32 v6, v6, v4
	v_mul_f32_e32 v7, v7, v4

.LBB0_891:
	s_or_b64 exec, exec, s[2:3]
	v_max_f32_e32 v0, v136, v135
	v_max3_f32 v0, v0, v99, v98
	v_max3_f32 v0, v0, v101, v100
	v_max3_f32 v0, v0, v95, v94
	v_max3_f32 v0, v0, v97, v96
	v_max3_f32 v0, v0, v91, v90
	v_max3_f32 v0, v0, v93, v92
	v_max3_f32 v0, v0, v87, v86
	v_mov_b32_e32 v2, v0
	s_nop 1
	v_permlane16_swap_b32_e32 v0, v2
	v_max_f32_e32 v0, v0, v2
	v_mov_b32_e32 v2, v0
	s_nop 1
	v_permlane32_swap_b32_e32 v0, v2
	v_max3_f32 v71, v133, v0, v2
	v_sub_f32_e32 v0, v133, v71
	v_exp_f32_e32 v2, v0
	s_nop 0
	v_cmp_neq_f32_e32 vcc, 1.0, v2
	s_cbranch_vccz .LBB0_893
	v_mul_f32_e32 v68, v68, v2
	v_mul_f32_e32 v69, v69, v2
	v_mul_f32_e32 v66, v66, v2
	v_mul_f32_e32 v67, v67, v2
	v_mul_f32_e32 v64, v64, v2
	v_mul_f32_e32 v65, v65, v2
	v_mul_f32_e32 v62, v62, v2
	v_mul_f32_e32 v63, v63, v2
	v_mul_f32_e32 v60, v60, v2
	v_mul_f32_e32 v61, v61, v2
	v_mul_f32_e32 v58, v58, v2
	v_mul_f32_e32 v59, v59, v2
	v_mul_f32_e32 v56, v56, v2
	v_mul_f32_e32 v57, v57, v2
	v_mul_f32_e32 v54, v54, v2
	v_mul_f32_e32 v55, v55, v2
	v_mul_f32_e32 v52, v52, v2
	v_mul_f32_e32 v53, v53, v2
	v_mul_f32_e32 v50, v50, v2
	v_mul_f32_e32 v51, v51, v2
	v_mul_f32_e32 v48, v48, v2
	v_mul_f32_e32 v49, v49, v2
	v_mul_f32_e32 v46, v46, v2
	v_mul_f32_e32 v47, v47, v2
	v_mul_f32_e32 v44, v44, v2
	v_mul_f32_e32 v45, v45, v2
	v_mul_f32_e32 v42, v42, v2
	v_mul_f32_e32 v43, v43, v2
	v_mul_f32_e32 v40, v40, v2
	v_mul_f32_e32 v41, v41, v2
	v_mul_f32_e32 v38, v38, v2
	v_mul_f32_e32 v39, v39, v2
